# loop rotated: the reduce falls through into layer 0, back edge sits before the reduce barrier; out-tile store after the lane exchange
# baseline (speedup 1.0000x reference)
.Lreduce:
	s_waitcnt lgkmcnt(0)
	s_barrier
	ds_read_b128 v[232:235], v113
	ds_read_b128 v[236:239], v113 offset:1024
	s_waitcnt lgkmcnt(0)
	v_add_f32_e32 v0, v232, v233
	v_add_f32_e32 v1, v234, v235
	v_add_f32_e32 v121, v236, v237
	v_add_f32_e32 v144, v238, v239
	v_add_f32_e32 v0, v0, v1
	v_add_f32_e32 v121, v121, v144
	v_add_f32_e32 v0, v0, v121
	v_add_f32_e32 v0, s30, v0
	v_cvt_f16_f32_e32 v1, v0
	v_cvt_f16_f32_e32 v121, v0
	s_nop 1
	v_permlane16_swap_b32_e32 v1, v121
	v_mov_b32_e32 v144, v1
	v_mov_b32_e32 v145, v121
	s_nop 1
	v_permlane32_swap_b32_e32 v1, v144
	v_permlane32_swap_b32_e32 v121, v145
	ds_write_b32 v106, v0
	v_add_u32_e32 v106, 4, v106
	s_cbranch_scc1 .LBB1_8
.LBB1_4:
	s_and_saveexec_b64 s[8:9], s[2:3]
	v_perm_b32 v5, v1, v102, s23
	v_perm_b32 v9, v121, v103, s23
	v_perm_b32 v17, v144, v115, s23
	v_perm_b32 v29, v145, v116, s23
	s_or_b64 exec, exec, s[8:9]
	v_mfma_f32_16x16x32_f16 v[164:167], v[30:33], v[2:5], 0
	v_mfma_f32_16x16x32_f16 v[180:183], v[22:25], v[2:5], 0
	s_cmp_lg_u32 s22, 0x818000
	v_mfma_f32_16x16x32_f16 v[168:171], v[30:33], v[6:9], 0
	v_mfma_f32_16x16x32_f16 v[184:187], v[22:25], v[6:9], 0
	s_cselect_b32 s9, s11, 15
	v_mfma_f32_16x16x32_f16 v[172:175], v[30:33], v[14:17], 0
	v_mfma_f32_16x16x32_f16 v[188:191], v[22:25], v[14:17], 0
	v_mfma_f32_16x16x32_f16 v[176:179], v[30:33], v[26:29], 0
	v_mfma_f32_16x16x32_f16 v[192:195], v[22:25], v[26:29], 0
	v_mfma_f32_16x16x32_f16 v[208:211], v[18:21], v[2:5], 0
	v_cvt_pk_f16_f32 v122, v164, v165
	v_cvt_pk_f16_f32 v123, v166, v167
	v_pk_max_f16 v122, v122, 0
	v_pk_max_f16 v123, v123, 0
	v_cvt_pk_f16_f32 v124, v180, v181
	v_cvt_pk_f16_f32 v125, v182, v183
	v_pk_max_f16 v124, v124, 0
	v_pk_max_f16 v125, v125, 0
	ds_write_b128 v107, v[122:125]
	v_mfma_f32_16x16x32_f16 v[224:227], v[10:13], v[2:5], 0
	v_cvt_pk_f16_f32 v126, v168, v169
	v_cvt_pk_f16_f32 v127, v170, v171
	v_pk_max_f16 v126, v126, 0
	v_pk_max_f16 v127, v127, 0
	v_cvt_pk_f16_f32 v128, v184, v185
	v_cvt_pk_f16_f32 v129, v186, v187
	v_pk_max_f16 v128, v128, 0
	v_pk_max_f16 v129, v129, 0
	ds_write_b128 v107, v[126:129] offset:16384
	v_mfma_f32_16x16x32_f16 v[212:215], v[18:21], v[6:9], 0
	v_cvt_pk_f16_f32 v134, v172, v173
	v_cvt_pk_f16_f32 v135, v174, v175
	v_pk_max_f16 v134, v134, 0
	v_pk_max_f16 v135, v135, 0
	v_cvt_pk_f16_f32 v136, v188, v189
	v_cvt_pk_f16_f32 v137, v190, v191
	v_pk_max_f16 v136, v136, 0
	v_pk_max_f16 v137, v137, 0
	ds_write_b128 v107, v[134:137] offset:32768
	v_mfma_f32_16x16x32_f16 v[228:231], v[10:13], v[6:9], 0
	v_cvt_pk_f16_f32 v138, v176, v177
	v_cvt_pk_f16_f32 v139, v178, v179
	v_pk_max_f16 v138, v138, 0
	v_pk_max_f16 v139, v139, 0
	v_cvt_pk_f16_f32 v140, v192, v193
	v_cvt_pk_f16_f32 v141, v194, v195
	v_pk_max_f16 v140, v140, 0
	v_pk_max_f16 v141, v141, 0
	ds_write_b128 v107, v[138:141] offset:49152
	v_mfma_f32_16x16x32_f16 v[216:219], v[18:21], v[14:17], 0
	v_mfma_f32_16x16x32_f16 v[232:235], v[10:13], v[14:17], 0
	v_mfma_f32_16x16x32_f16 v[220:223], v[18:21], v[26:29], 0
	v_mfma_f32_16x16x32_f16 v[236:239], v[10:13], v[26:29], 0
	v_add_u32_e32 v111, s64, v111
	v_add_u32_e32 v98, s65, v98
	s_lshl_b32 s20, s9, 7
	v_lshl_add_u64 v[0:1], s[20:21], 3, v[132:133]
	s_add_i32 s25, s22, s34
	s_lshl_b32 s8, s9, 8
	buffer_load_dwordx4 v[192:195], v147, s[16:19], s25 offen
	buffer_load_dwordx4 v[196:199], v148, s[16:19], s25 offen
	buffer_load_dwordx4 v[200:203], v149, s[16:19], s25 offen
	buffer_load_dwordx4 v[204:207], v150, s[16:19], s25 offen
	s_waitcnt vmcnt(19)
	v_mfma_f32_16x16x32_f16 v[164:167], v[58:61], v[122:125], v[240:243]
	v_cvt_pk_f16_f32 v142, v208, v209
	v_cvt_pk_f16_f32 v143, v210, v211
	v_mfma_f32_16x16x32_f16 v[168:171], v[58:61], v[126:129], v[240:243]
	v_pk_max_f16 v142, v142, 0
	v_pk_max_f16 v143, v143, 0
	v_mfma_f32_16x16x32_f16 v[172:175], v[58:61], v[134:137], v[240:243]
	v_cvt_pk_f16_f32 v144, v224, v225
	v_cvt_pk_f16_f32 v145, v226, v227
	v_mfma_f32_16x16x32_f16 v[10:13], v[58:61], v[138:141], v[240:243]
	v_pk_max_f16 v144, v144, 0
	v_pk_max_f16 v145, v145, 0
	ds_write_b128 v108, v[142:145]
	s_waitcnt vmcnt(18)
	v_mfma_f32_16x16x32_f16 v[58:61], v[54:57], v[122:125], v[244:247]
	v_cvt_pk_f16_f32 v152, v212, v213
	v_cvt_pk_f16_f32 v153, v214, v215
	v_mfma_f32_16x16x32_f16 v[176:179], v[54:57], v[126:129], v[244:247]
	v_pk_max_f16 v152, v152, 0
	v_pk_max_f16 v153, v153, 0
	v_mfma_f32_16x16x32_f16 v[180:183], v[54:57], v[134:137], v[244:247]
	v_cvt_pk_f16_f32 v154, v228, v229
	v_cvt_pk_f16_f32 v155, v230, v231
	v_mfma_f32_16x16x32_f16 v[18:21], v[54:57], v[138:141], v[244:247]
	v_pk_max_f16 v154, v154, 0
	v_pk_max_f16 v155, v155, 0
	ds_write_b128 v108, v[152:155] offset:16384
	s_waitcnt vmcnt(17)
	v_mfma_f32_16x16x32_f16 v[54:57], v[50:53], v[122:125], v[248:251]
	v_cvt_pk_f16_f32 v156, v216, v217
	v_cvt_pk_f16_f32 v157, v218, v219
	v_mfma_f32_16x16x32_f16 v[184:187], v[50:53], v[126:129], v[248:251]
	v_pk_max_f16 v156, v156, 0
	v_pk_max_f16 v157, v157, 0
	v_mfma_f32_16x16x32_f16 v[188:191], v[50:53], v[134:137], v[248:251]
	v_cvt_pk_f16_f32 v158, v232, v233
	v_cvt_pk_f16_f32 v159, v234, v235
	v_mfma_f32_16x16x32_f16 v[22:25], v[50:53], v[138:141], v[248:251]
	v_pk_max_f16 v158, v158, 0
	v_pk_max_f16 v159, v159, 0
	ds_write_b128 v108, v[156:159] offset:32768
	s_waitcnt vmcnt(16)
	v_mfma_f32_16x16x32_f16 v[50:53], v[38:41], v[122:125], v[252:255]
	v_cvt_pk_f16_f32 v160, v220, v221
	v_cvt_pk_f16_f32 v161, v222, v223
	v_mfma_f32_16x16x32_f16 v[122:125], v[38:41], v[126:129], v[252:255]
	v_pk_max_f16 v160, v160, 0
	v_pk_max_f16 v161, v161, 0
	v_mfma_f32_16x16x32_f16 v[126:129], v[38:41], v[134:137], v[252:255]
	v_cvt_pk_f16_f32 v162, v236, v237
	v_cvt_pk_f16_f32 v163, v238, v239
	v_mfma_f32_16x16x32_f16 v[38:41], v[38:41], v[138:141], v[252:255]
	v_pk_max_f16 v162, v162, 0
	v_pk_max_f16 v163, v163, 0
	ds_write_b128 v108, v[160:163] offset:49152
	s_add_i32 s9, s22, s35
	s_waitcnt vmcnt(15)
	v_mfma_f32_16x16x32_f16 v[164:167], v[94:97], v[142:145], v[164:167]
	v_mfma_f32_16x16x32_f16 v[168:171], v[94:97], v[152:155], v[168:171]
	s_waitcnt vmcnt(14)
	v_mfma_f32_16x16x32_f16 v[58:61], v[90:93], v[142:145], v[58:61]
	v_mfma_f32_16x16x32_f16 v[176:179], v[90:93], v[152:155], v[176:179]
	s_waitcnt vmcnt(13)
	v_mfma_f32_16x16x32_f16 v[54:57], v[78:81], v[142:145], v[54:57]
	v_mfma_f32_16x16x32_f16 v[184:187], v[78:81], v[152:155], v[184:187]
	s_waitcnt vmcnt(12)
	v_mfma_f32_16x16x32_f16 v[50:53], v[34:37], v[142:145], v[50:53]
	buffer_load_dwordx4 v[140:143], v147, s[16:19], s9 offen
	buffer_load_dwordx4 v[220:223], v148, s[16:19], s9 offen
	v_mfma_f32_16x16x32_f16 v[122:125], v[34:37], v[152:155], v[122:125]
	buffer_load_dwordx4 v[152:155], v149, s[16:19], s9 offen
	buffer_load_dwordx4 v[224:227], v150, s[16:19], s9 offen
	s_mov_b32 s9, s21
	s_waitcnt lgkmcnt(0)
	s_barrier
	v_add_u32_e32 v99, s66, v99
	ds_read_b128 v[136:139], v99
	ds_read_b128 v[208:211], v99 offset:16384
	ds_read_b128 v[212:215], v99 offset:32768
	ds_read_b128 v[216:219], v99 offset:49152
	v_mfma_f32_16x16x32_f16 v[172:175], v[94:97], v[156:159], v[172:175]
	v_mfma_f32_16x16x32_f16 v[94:97], v[94:97], v[160:163], v[10:13]
	s_nop 2
	v_lshl_add_u64 v[10:11], s[8:9], 4, v[130:131]
	v_mfma_f32_16x16x32_f16 v[180:183], v[90:93], v[156:159], v[180:183]
	v_mfma_f32_16x16x32_f16 v[90:93], v[90:93], v[160:163], v[18:21]
	v_mfma_f32_16x16x32_f16 v[188:191], v[78:81], v[156:159], v[188:191]
	v_mfma_f32_16x16x32_f16 v[78:81], v[78:81], v[160:163], v[22:25]
	global_load_dwordx4 v[30:33], v[10:11], off
	s_nop 1
	global_load_dwordx4 v[22:25], v[10:11], off offset:1024
	global_load_dwordx4 v[18:21], v[10:11], off offset:2048
	s_nop 0
	global_load_dwordx4 v[10:13], v[10:11], off offset:3072
	s_nop 0
	global_load_dwordx2 v[134:135], v[0:1], off
	v_mfma_f32_16x16x32_f16 v[126:129], v[34:37], v[156:159], v[126:129]
	v_mfma_f32_16x16x32_f16 v[34:37], v[34:37], v[160:163], v[38:41]
	s_nop 2
	v_add_u32_e32 v100, s67, v100
	ds_read_b128 v[38:41], v100
	ds_read_b128 v[156:159], v100 offset:16384
	ds_read_b128 v[160:163], v100 offset:32768
	ds_read_b128 v[228:231], v100 offset:49152
	s_add_i32 s8, s22, s36
	s_waitcnt vmcnt(20) lgkmcnt(7)
	v_mfma_f32_16x16x32_f16 v[164:167], v[82:85], v[136:139], v[164:167]
	s_waitcnt lgkmcnt(6)
	v_mfma_f32_16x16x32_f16 v[168:171], v[82:85], v[208:211], v[168:171]
	s_waitcnt lgkmcnt(5)
	v_mfma_f32_16x16x32_f16 v[172:175], v[82:85], v[212:215], v[172:175]
	s_waitcnt lgkmcnt(4)
	v_mfma_f32_16x16x32_f16 v[82:85], v[82:85], v[216:219], v[94:97]
	s_waitcnt vmcnt(19)
	v_mfma_f32_16x16x32_f16 v[58:61], v[70:73], v[136:139], v[58:61]
	v_mfma_f32_16x16x32_f16 v[94:97], v[70:73], v[208:211], v[176:179]
	v_mfma_f32_16x16x32_f16 v[176:179], v[70:73], v[212:215], v[180:183]
	v_mfma_f32_16x16x32_f16 v[70:73], v[70:73], v[216:219], v[90:93]
	s_waitcnt vmcnt(18)
	v_mfma_f32_16x16x32_f16 v[54:57], v[62:65], v[136:139], v[54:57]
	v_mfma_f32_16x16x32_f16 v[90:93], v[62:65], v[208:211], v[184:187]
	v_mfma_f32_16x16x32_f16 v[180:183], v[62:65], v[212:215], v[188:191]
	v_mfma_f32_16x16x32_f16 v[62:65], v[62:65], v[216:219], v[78:81]
	s_waitcnt vmcnt(17)
	v_mfma_f32_16x16x32_f16 v[50:53], v[42:45], v[136:139], v[50:53]
	v_mfma_f32_16x16x32_f16 v[78:81], v[42:45], v[208:211], v[122:125]
	v_mfma_f32_16x16x32_f16 v[122:125], v[42:45], v[212:215], v[126:129]
	s_nop 2
	buffer_load_dwordx4 v[126:129], v147, s[16:19], s8 offen
	buffer_load_dwordx4 v[136:139], v148, s[16:19], s8 offen
	buffer_load_dwordx4 v[184:187], v149, s[16:19], s8 offen
	buffer_load_dwordx4 v[188:191], v150, s[16:19], s8 offen
	v_mfma_f32_16x16x32_f16 v[34:37], v[42:45], v[216:219], v[34:37]
	v_add_u32_e32 v111, s68, v111
	ds_read_b128 v[42:45], v111
	ds_read_b128 v[208:211], v111 offset:16384
	ds_read_b128 v[212:215], v111 offset:32768
	ds_read_b128 v[216:219], v111 offset:49152
	s_add_i32 s8, s22, s37
	s_waitcnt vmcnt(20) lgkmcnt(7)
	v_mfma_f32_16x16x32_f16 v[164:167], v[86:89], v[38:41], v[164:167]
	s_waitcnt lgkmcnt(6)
	v_mfma_f32_16x16x32_f16 v[168:171], v[86:89], v[156:159], v[168:171]
	s_waitcnt lgkmcnt(5)
	v_mfma_f32_16x16x32_f16 v[172:175], v[86:89], v[160:163], v[172:175]
	s_waitcnt lgkmcnt(4)
	v_mfma_f32_16x16x32_f16 v[82:85], v[86:89], v[228:231], v[82:85]
	s_waitcnt vmcnt(19)
	v_mfma_f32_16x16x32_f16 v[58:61], v[74:77], v[38:41], v[58:61]
	v_mfma_f32_16x16x32_f16 v[86:89], v[74:77], v[156:159], v[94:97]
	v_mfma_f32_16x16x32_f16 v[94:97], v[74:77], v[160:163], v[176:179]
	v_mfma_f32_16x16x32_f16 v[70:73], v[74:77], v[228:231], v[70:73]
	s_waitcnt vmcnt(18)
	v_mfma_f32_16x16x32_f16 v[54:57], v[66:69], v[38:41], v[54:57]
	v_mfma_f32_16x16x32_f16 v[74:77], v[66:69], v[156:159], v[90:93]
	v_mfma_f32_16x16x32_f16 v[90:93], v[66:69], v[160:163], v[180:183]
	v_mfma_f32_16x16x32_f16 v[62:65], v[66:69], v[228:231], v[62:65]
	s_waitcnt vmcnt(17)
	v_mfma_f32_16x16x32_f16 v[38:41], v[46:49], v[38:41], v[50:53]
	v_mfma_f32_16x16x32_f16 v[50:53], v[46:49], v[156:159], v[78:81]
	v_mfma_f32_16x16x32_f16 v[66:69], v[46:49], v[160:163], v[122:125]
	s_nop 1
	buffer_load_dwordx4 v[78:81], v147, s[16:19], s8 offen
	buffer_load_dwordx4 v[122:125], v148, s[16:19], s8 offen
	buffer_load_dwordx4 v[156:159], v149, s[16:19], s8 offen
	buffer_load_dwordx4 v[160:163], v150, s[16:19], s8 offen
	v_mfma_f32_16x16x32_f16 v[34:37], v[46:49], v[228:231], v[34:37]
	v_add_u32_e32 v98, s69, v98
	ds_read_b128 v[46:49], v98
	ds_read_b128 v[176:179], v98 offset:16384
	ds_read_b128 v[180:183], v98 offset:32768
	ds_read_b128 v[228:231], v98 offset:49152
	s_add_i32 s8, s22, s38
	s_waitcnt vmcnt(20) lgkmcnt(7)
	v_mfma_f32_16x16x32_f16 v[164:167], v[192:195], v[42:45], v[164:167]
	s_waitcnt lgkmcnt(6)
	v_mfma_f32_16x16x32_f16 v[168:171], v[192:195], v[208:211], v[168:171]
	s_waitcnt lgkmcnt(5)
	v_mfma_f32_16x16x32_f16 v[172:175], v[192:195], v[212:215], v[172:175]
	s_waitcnt lgkmcnt(4)
	v_mfma_f32_16x16x32_f16 v[82:85], v[192:195], v[216:219], v[82:85]
	s_waitcnt vmcnt(19)
	v_mfma_f32_16x16x32_f16 v[58:61], v[196:199], v[42:45], v[58:61]
	v_mfma_f32_16x16x32_f16 v[86:89], v[196:199], v[208:211], v[86:89]
	v_mfma_f32_16x16x32_f16 v[94:97], v[196:199], v[212:215], v[94:97]
	v_mfma_f32_16x16x32_f16 v[70:73], v[196:199], v[216:219], v[70:73]
	s_waitcnt vmcnt(18)
	v_mfma_f32_16x16x32_f16 v[54:57], v[200:203], v[42:45], v[54:57]
	v_mfma_f32_16x16x32_f16 v[74:77], v[200:203], v[208:211], v[74:77]
	v_mfma_f32_16x16x32_f16 v[90:93], v[200:203], v[212:215], v[90:93]
	v_mfma_f32_16x16x32_f16 v[62:65], v[200:203], v[216:219], v[62:65]
	s_waitcnt vmcnt(17)
	v_mfma_f32_16x16x32_f16 v[38:41], v[204:207], v[42:45], v[38:41]
	v_mfma_f32_16x16x32_f16 v[42:45], v[204:207], v[208:211], v[50:53]
	v_mfma_f32_16x16x32_f16 v[50:53], v[204:207], v[212:215], v[66:69]
	s_nop 2
	buffer_load_dwordx4 v[66:69], v147, s[16:19], s8 offen
	buffer_load_dwordx4 v[192:195], v148, s[16:19], s8 offen
	buffer_load_dwordx4 v[196:199], v149, s[16:19], s8 offen
	buffer_load_dwordx4 v[200:203], v150, s[16:19], s8 offen
	v_mfma_f32_16x16x32_f16 v[34:37], v[204:207], v[216:219], v[34:37]
	v_add_u32_e32 v99, s70, v99
	ds_read_b128 v[204:207], v99
	ds_read_b128 v[208:211], v99 offset:16384
	ds_read_b128 v[212:215], v99 offset:32768
	ds_read_b128 v[216:219], v99 offset:49152
	s_add_i32 s8, s22, s39
	s_waitcnt vmcnt(20) lgkmcnt(7)
	v_mfma_f32_16x16x32_f16 v[164:167], v[140:143], v[46:49], v[164:167]
	s_waitcnt lgkmcnt(6)
	v_mfma_f32_16x16x32_f16 v[168:171], v[140:143], v[176:179], v[168:171]
	s_waitcnt lgkmcnt(5)
	v_mfma_f32_16x16x32_f16 v[172:175], v[140:143], v[180:183], v[172:175]
	s_waitcnt lgkmcnt(4)
	v_mfma_f32_16x16x32_f16 v[82:85], v[140:143], v[228:231], v[82:85]
	s_waitcnt vmcnt(19)
	v_mfma_f32_16x16x32_f16 v[58:61], v[220:223], v[46:49], v[58:61]
	v_mfma_f32_16x16x32_f16 v[86:89], v[220:223], v[176:179], v[86:89]
	s_waitcnt vmcnt(18)
	v_mfma_f32_16x16x32_f16 v[54:57], v[152:155], v[46:49], v[54:57]
	v_mfma_f32_16x16x32_f16 v[74:77], v[152:155], v[176:179], v[74:77]
	v_mfma_f32_16x16x32_f16 v[90:93], v[152:155], v[180:183], v[90:93]
	v_mfma_f32_16x16x32_f16 v[62:65], v[152:155], v[228:231], v[62:65]
	s_waitcnt vmcnt(17)
	v_mfma_f32_16x16x32_f16 v[38:41], v[224:227], v[46:49], v[38:41]
	v_mfma_f32_16x16x32_f16 v[42:45], v[224:227], v[176:179], v[42:45]
	v_mfma_f32_16x16x32_f16 v[46:49], v[224:227], v[180:183], v[50:53]
	s_nop 2
	buffer_load_dwordx4 v[50:53], v147, s[16:19], s8 offen
	buffer_load_dwordx4 v[140:143], v148, s[16:19], s8 offen
	buffer_load_dwordx4 v[152:155], v149, s[16:19], s8 offen
	buffer_load_dwordx4 v[176:179], v150, s[16:19], s8 offen
	v_mfma_f32_16x16x32_f16 v[94:97], v[220:223], v[180:183], v[94:97]
	v_mfma_f32_16x16x32_f16 v[70:73], v[220:223], v[228:231], v[70:73]
	v_mfma_f32_16x16x32_f16 v[34:37], v[224:227], v[228:231], v[34:37]
	v_add_u32_e32 v100, s71, v100
	ds_read_b128 v[180:183], v100
	ds_read_b128 v[220:223], v100 offset:16384
	ds_read_b128 v[224:227], v100 offset:32768
	ds_read_b128 v[228:231], v100 offset:49152
	s_add_i32 s8, s22, s40
	s_waitcnt vmcnt(15) lgkmcnt(7)
	v_mfma_f32_16x16x32_f16 v[164:167], v[126:129], v[204:207], v[164:167]
	s_waitcnt lgkmcnt(6)
	v_mfma_f32_16x16x32_f16 v[168:171], v[126:129], v[208:211], v[168:171]
	s_waitcnt lgkmcnt(5)
	v_mfma_f32_16x16x32_f16 v[172:175], v[126:129], v[212:215], v[172:175]
	s_waitcnt lgkmcnt(4)
	v_mfma_f32_16x16x32_f16 v[82:85], v[126:129], v[216:219], v[82:85]
	s_waitcnt vmcnt(14)
	v_mfma_f32_16x16x32_f16 v[58:61], v[136:139], v[204:207], v[58:61]
	v_mfma_f32_16x16x32_f16 v[86:89], v[136:139], v[208:211], v[86:89]
	v_mfma_f32_16x16x32_f16 v[94:97], v[136:139], v[212:215], v[94:97]
	v_mfma_f32_16x16x32_f16 v[70:73], v[136:139], v[216:219], v[70:73]
	s_waitcnt vmcnt(13)
	v_mfma_f32_16x16x32_f16 v[54:57], v[184:187], v[204:207], v[54:57]
	v_mfma_f32_16x16x32_f16 v[74:77], v[184:187], v[208:211], v[74:77]
	v_mfma_f32_16x16x32_f16 v[90:93], v[184:187], v[212:215], v[90:93]
	v_mfma_f32_16x16x32_f16 v[62:65], v[184:187], v[216:219], v[62:65]
	s_waitcnt vmcnt(12)
	v_mfma_f32_16x16x32_f16 v[38:41], v[188:191], v[204:207], v[38:41]
	buffer_load_dwordx4 v[126:129], v147, s[16:19], s8 offen
	buffer_load_dwordx4 v[136:139], v148, s[16:19], s8 offen
	buffer_load_dwordx4 v[184:187], v149, s[16:19], s8 offen
	buffer_load_dwordx4 v[204:207], v150, s[16:19], s8 offen
	v_mfma_f32_16x16x32_f16 v[42:45], v[188:191], v[208:211], v[42:45]
	v_mfma_f32_16x16x32_f16 v[46:49], v[188:191], v[212:215], v[46:49]
	v_mfma_f32_16x16x32_f16 v[34:37], v[188:191], v[216:219], v[34:37]
	v_add_u32_e32 v111, s72, v111
	ds_read_b128 v[188:191], v111
	ds_read_b128 v[208:211], v111 offset:16384
	ds_read_b128 v[212:215], v111 offset:32768
	ds_read_b128 v[216:219], v111 offset:49152
	s_add_i32 s8, s22, s41
	s_waitcnt vmcnt(15) lgkmcnt(7)
	v_mfma_f32_16x16x32_f16 v[164:167], v[78:81], v[180:183], v[164:167]
	s_waitcnt lgkmcnt(6)
	v_mfma_f32_16x16x32_f16 v[168:171], v[78:81], v[220:223], v[168:171]
	s_waitcnt lgkmcnt(5)
	v_mfma_f32_16x16x32_f16 v[172:175], v[78:81], v[224:227], v[172:175]
	s_waitcnt lgkmcnt(4)
	v_mfma_f32_16x16x32_f16 v[78:81], v[78:81], v[228:231], v[82:85]
	s_waitcnt vmcnt(14)
	v_mfma_f32_16x16x32_f16 v[58:61], v[122:125], v[180:183], v[58:61]
	v_mfma_f32_16x16x32_f16 v[82:85], v[122:125], v[220:223], v[86:89]
	v_mfma_f32_16x16x32_f16 v[86:89], v[122:125], v[224:227], v[94:97]
	v_mfma_f32_16x16x32_f16 v[70:73], v[122:125], v[228:231], v[70:73]
	s_waitcnt vmcnt(13)
	v_mfma_f32_16x16x32_f16 v[54:57], v[156:159], v[180:183], v[54:57]
	v_mfma_f32_16x16x32_f16 v[74:77], v[156:159], v[220:223], v[74:77]
	v_mfma_f32_16x16x32_f16 v[90:93], v[156:159], v[224:227], v[90:93]
	v_mfma_f32_16x16x32_f16 v[62:65], v[156:159], v[228:231], v[62:65]
	s_waitcnt vmcnt(12)
	v_mfma_f32_16x16x32_f16 v[38:41], v[160:163], v[180:183], v[38:41]
	buffer_load_dwordx4 v[94:97], v147, s[16:19], s8 offen
	buffer_load_dwordx4 v[122:125], v148, s[16:19], s8 offen
	buffer_load_dwordx4 v[156:159], v149, s[16:19], s8 offen
	buffer_load_dwordx4 v[180:183], v150, s[16:19], s8 offen
	v_mfma_f32_16x16x32_f16 v[42:45], v[160:163], v[220:223], v[42:45]
	v_mfma_f32_16x16x32_f16 v[46:49], v[160:163], v[224:227], v[46:49]
	v_mfma_f32_16x16x32_f16 v[34:37], v[160:163], v[228:231], v[34:37]
	v_add_u32_e32 v98, s73, v98
	ds_read_b128 v[160:163], v98
	ds_read_b128 v[220:223], v98 offset:16384
	ds_read_b128 v[224:227], v98 offset:32768
	ds_read_b128 v[228:231], v98 offset:49152
	s_add_i32 s8, s22, s42
	s_waitcnt vmcnt(15) lgkmcnt(7)
	v_mfma_f32_16x16x32_f16 v[164:167], v[66:69], v[188:191], v[164:167]
	s_waitcnt lgkmcnt(6)
	v_mfma_f32_16x16x32_f16 v[168:171], v[66:69], v[208:211], v[168:171]
	s_waitcnt lgkmcnt(5)
	v_mfma_f32_16x16x32_f16 v[172:175], v[66:69], v[212:215], v[172:175]
	s_waitcnt lgkmcnt(4)
	v_mfma_f32_16x16x32_f16 v[66:69], v[66:69], v[216:219], v[78:81]
	s_waitcnt vmcnt(14)
	v_mfma_f32_16x16x32_f16 v[58:61], v[192:195], v[188:191], v[58:61]
	v_mfma_f32_16x16x32_f16 v[78:81], v[192:195], v[208:211], v[82:85]
	v_mfma_f32_16x16x32_f16 v[82:85], v[192:195], v[212:215], v[86:89]
	v_mfma_f32_16x16x32_f16 v[70:73], v[192:195], v[216:219], v[70:73]
	s_waitcnt vmcnt(13)
	v_mfma_f32_16x16x32_f16 v[54:57], v[196:199], v[188:191], v[54:57]
	v_mfma_f32_16x16x32_f16 v[74:77], v[196:199], v[208:211], v[74:77]
	v_mfma_f32_16x16x32_f16 v[86:89], v[196:199], v[212:215], v[90:93]
	v_mfma_f32_16x16x32_f16 v[62:65], v[196:199], v[216:219], v[62:65]
	s_waitcnt vmcnt(12)
	v_mfma_f32_16x16x32_f16 v[38:41], v[200:203], v[188:191], v[38:41]
	buffer_load_dwordx4 v[90:93], v147, s[16:19], s8 offen
	buffer_load_dwordx4 v[188:191], v148, s[16:19], s8 offen
	buffer_load_dwordx4 v[192:195], v149, s[16:19], s8 offen
	buffer_load_dwordx4 v[196:199], v150, s[16:19], s8 offen
	v_mfma_f32_16x16x32_f16 v[42:45], v[200:203], v[208:211], v[42:45]
	v_mfma_f32_16x16x32_f16 v[46:49], v[200:203], v[212:215], v[46:49]
	v_mfma_f32_16x16x32_f16 v[34:37], v[200:203], v[216:219], v[34:37]
	v_add_u32_e32 v99, s74, v99
	ds_read_b128 v[200:203], v99
	ds_read_b128 v[208:211], v99 offset:16384
	ds_read_b128 v[212:215], v99 offset:32768
	ds_read_b128 v[216:219], v99 offset:49152
	s_add_i32 s8, s22, s43
	s_waitcnt vmcnt(15) lgkmcnt(7)
	v_mfma_f32_16x16x32_f16 v[164:167], v[50:53], v[160:163], v[164:167]
	s_waitcnt lgkmcnt(6)
	v_mfma_f32_16x16x32_f16 v[168:171], v[50:53], v[220:223], v[168:171]
	s_waitcnt lgkmcnt(5)
	v_mfma_f32_16x16x32_f16 v[172:175], v[50:53], v[224:227], v[172:175]
	s_waitcnt lgkmcnt(4)
	v_mfma_f32_16x16x32_f16 v[50:53], v[50:53], v[228:231], v[66:69]
	s_waitcnt vmcnt(14)
	v_mfma_f32_16x16x32_f16 v[58:61], v[140:143], v[160:163], v[58:61]
	v_mfma_f32_16x16x32_f16 v[66:69], v[140:143], v[220:223], v[78:81]
	v_mfma_f32_16x16x32_f16 v[78:81], v[140:143], v[224:227], v[82:85]
	v_mfma_f32_16x16x32_f16 v[70:73], v[140:143], v[228:231], v[70:73]
	s_waitcnt vmcnt(13)
	v_mfma_f32_16x16x32_f16 v[54:57], v[152:155], v[160:163], v[54:57]
	v_mfma_f32_16x16x32_f16 v[74:77], v[152:155], v[220:223], v[74:77]
	v_mfma_f32_16x16x32_f16 v[82:85], v[152:155], v[224:227], v[86:89]
	v_mfma_f32_16x16x32_f16 v[62:65], v[152:155], v[228:231], v[62:65]
	s_waitcnt vmcnt(12)
	v_mfma_f32_16x16x32_f16 v[38:41], v[176:179], v[160:163], v[38:41]
	buffer_load_dwordx4 v[86:89], v147, s[16:19], s8 offen
	buffer_load_dwordx4 v[140:143], v148, s[16:19], s8 offen
	buffer_load_dwordx4 v[152:155], v149, s[16:19], s8 offen
	buffer_load_dwordx4 v[160:163], v150, s[16:19], s8 offen
	v_mfma_f32_16x16x32_f16 v[42:45], v[176:179], v[220:223], v[42:45]
	v_mfma_f32_16x16x32_f16 v[46:49], v[176:179], v[224:227], v[46:49]
	v_mfma_f32_16x16x32_f16 v[34:37], v[176:179], v[228:231], v[34:37]
	v_add_u32_e32 v100, s75, v100
	ds_read_b128 v[176:179], v100
	ds_read_b128 v[220:223], v100 offset:16384
	ds_read_b128 v[224:227], v100 offset:32768
	ds_read_b128 v[228:231], v100 offset:49152
	s_add_i32 s8, s22, s44
	s_waitcnt vmcnt(15) lgkmcnt(7)
	v_mfma_f32_16x16x32_f16 v[164:167], v[126:129], v[200:203], v[164:167]
	s_waitcnt lgkmcnt(6)
	v_mfma_f32_16x16x32_f16 v[168:171], v[126:129], v[208:211], v[168:171]
	s_waitcnt lgkmcnt(5)
	v_mfma_f32_16x16x32_f16 v[172:175], v[126:129], v[212:215], v[172:175]
	s_waitcnt lgkmcnt(4)
	v_mfma_f32_16x16x32_f16 v[50:53], v[126:129], v[216:219], v[50:53]
	s_waitcnt vmcnt(14)
	v_mfma_f32_16x16x32_f16 v[58:61], v[136:139], v[200:203], v[58:61]
	v_mfma_f32_16x16x32_f16 v[66:69], v[136:139], v[208:211], v[66:69]
	v_mfma_f32_16x16x32_f16 v[78:81], v[136:139], v[212:215], v[78:81]
	v_mfma_f32_16x16x32_f16 v[70:73], v[136:139], v[216:219], v[70:73]
	s_waitcnt vmcnt(13)
	v_mfma_f32_16x16x32_f16 v[54:57], v[184:187], v[200:203], v[54:57]
	v_mfma_f32_16x16x32_f16 v[74:77], v[184:187], v[208:211], v[74:77]
	v_mfma_f32_16x16x32_f16 v[82:85], v[184:187], v[212:215], v[82:85]
	v_mfma_f32_16x16x32_f16 v[62:65], v[184:187], v[216:219], v[62:65]
	s_waitcnt vmcnt(12)
	v_mfma_f32_16x16x32_f16 v[38:41], v[204:207], v[200:203], v[38:41]
	buffer_load_dwordx4 v[126:129], v147, s[16:19], s8 offen
	buffer_load_dwordx4 v[136:139], v148, s[16:19], s8 offen
	buffer_load_dwordx4 v[184:187], v149, s[16:19], s8 offen
	buffer_load_dwordx4 v[200:203], v150, s[16:19], s8 offen
	v_mfma_f32_16x16x32_f16 v[42:45], v[204:207], v[208:211], v[42:45]
	v_mfma_f32_16x16x32_f16 v[46:49], v[204:207], v[212:215], v[46:49]
	v_mfma_f32_16x16x32_f16 v[34:37], v[204:207], v[216:219], v[34:37]
	v_add_u32_e32 v111, s76, v111
	ds_read_b128 v[204:207], v111
	ds_read_b128 v[208:211], v111 offset:16384
	ds_read_b128 v[212:215], v111 offset:32768
	ds_read_b128 v[216:219], v111 offset:49152
	s_add_i32 s8, s22, s45
	s_waitcnt vmcnt(15) lgkmcnt(7)
	v_mfma_f32_16x16x32_f16 v[164:167], v[94:97], v[176:179], v[164:167]
	s_waitcnt lgkmcnt(6)
	v_mfma_f32_16x16x32_f16 v[168:171], v[94:97], v[220:223], v[168:171]
	s_waitcnt vmcnt(14)
	v_mfma_f32_16x16x32_f16 v[58:61], v[122:125], v[176:179], v[58:61]
	v_mfma_f32_16x16x32_f16 v[66:69], v[122:125], v[220:223], v[66:69]
	s_waitcnt lgkmcnt(5)
	v_mfma_f32_16x16x32_f16 v[78:81], v[122:125], v[224:227], v[78:81]
	s_waitcnt lgkmcnt(4)
	v_mfma_f32_16x16x32_f16 v[70:73], v[122:125], v[228:231], v[70:73]
	s_waitcnt vmcnt(13)
	v_mfma_f32_16x16x32_f16 v[54:57], v[156:159], v[176:179], v[54:57]
	v_mfma_f32_16x16x32_f16 v[74:77], v[156:159], v[220:223], v[74:77]
	v_mfma_f32_16x16x32_f16 v[82:85], v[156:159], v[224:227], v[82:85]
	v_mfma_f32_16x16x32_f16 v[62:65], v[156:159], v[228:231], v[62:65]
	s_waitcnt vmcnt(12)
	v_mfma_f32_16x16x32_f16 v[38:41], v[180:183], v[176:179], v[38:41]
	v_mfma_f32_16x16x32_f16 v[42:45], v[180:183], v[220:223], v[42:45]
	buffer_load_dwordx4 v[122:125], v147, s[16:19], s8 offen
	buffer_load_dwordx4 v[156:159], v148, s[16:19], s8 offen
	buffer_load_dwordx4 v[176:179], v149, s[16:19], s8 offen
	buffer_load_dwordx4 v[220:223], v150, s[16:19], s8 offen
	v_mfma_f32_16x16x32_f16 v[50:53], v[94:97], v[228:231], v[50:53]
	v_mfma_f32_16x16x32_f16 v[46:49], v[180:183], v[224:227], v[46:49]
	v_mfma_f32_16x16x32_f16 v[34:37], v[180:183], v[228:231], v[34:37]
	v_mfma_f32_16x16x32_f16 v[172:175], v[94:97], v[224:227], v[172:175]
	v_add_u32_e32 v98, s77, v98
	ds_read_b128 v[94:97], v98
	ds_read_b128 v[180:183], v98 offset:16384
	ds_read_b128 v[224:227], v98 offset:32768
	ds_read_b128 v[228:231], v98 offset:49152
	s_add_i32 s8, s22, s46
	s_waitcnt vmcnt(15) lgkmcnt(7)
	v_mfma_f32_16x16x32_f16 v[164:167], v[90:93], v[204:207], v[164:167]
	s_waitcnt lgkmcnt(6)
	v_mfma_f32_16x16x32_f16 v[168:171], v[90:93], v[208:211], v[168:171]
	s_waitcnt lgkmcnt(5)
	v_mfma_f32_16x16x32_f16 v[172:175], v[90:93], v[212:215], v[172:175]
	s_waitcnt lgkmcnt(4)
	v_mfma_f32_16x16x32_f16 v[90:93], v[90:93], v[216:219], v[50:53]
	s_waitcnt vmcnt(14)
	v_mfma_f32_16x16x32_f16 v[232:235], v[188:191], v[204:207], v[58:61]
	v_mfma_f32_16x16x32_f16 v[66:69], v[188:191], v[208:211], v[66:69]
	v_mfma_f32_16x16x32_f16 v[78:81], v[188:191], v[212:215], v[78:81]
	v_mfma_f32_16x16x32_f16 v[70:73], v[188:191], v[216:219], v[70:73]
	s_waitcnt vmcnt(13)
	v_mfma_f32_16x16x32_f16 v[188:191], v[192:195], v[204:207], v[54:57]
	v_mfma_f32_16x16x32_f16 v[74:77], v[192:195], v[208:211], v[74:77]
	v_mfma_f32_16x16x32_f16 v[82:85], v[192:195], v[212:215], v[82:85]
	v_mfma_f32_16x16x32_f16 v[62:65], v[192:195], v[216:219], v[62:65]
	s_waitcnt vmcnt(12)
	v_mfma_f32_16x16x32_f16 v[192:195], v[196:199], v[204:207], v[38:41]
	buffer_load_dwordx4 v[58:61], v147, s[16:19], s8 offen
	buffer_load_dwordx4 v[54:57], v148, s[16:19], s8 offen
	buffer_load_dwordx4 v[50:53], v149, s[16:19], s8 offen
	buffer_load_dwordx4 v[38:41], v150, s[16:19], s8 offen
	v_mfma_f32_16x16x32_f16 v[42:45], v[196:199], v[208:211], v[42:45]
	v_mfma_f32_16x16x32_f16 v[46:49], v[196:199], v[212:215], v[46:49]
	v_mfma_f32_16x16x32_f16 v[196:199], v[196:199], v[216:219], v[34:37]
	v_add_u32_e32 v99, s78, v99
	ds_read_b128 v[204:207], v99
	ds_read_b128 v[208:211], v99 offset:16384
	ds_read_b128 v[212:215], v99 offset:32768
	ds_read_b128 v[216:219], v99 offset:49152
	s_add_i32 s8, s22, s47
	s_waitcnt vmcnt(15) lgkmcnt(7)
	v_mfma_f32_16x16x32_f16 v[164:167], v[86:89], v[94:97], v[164:167]
	s_waitcnt lgkmcnt(6)
	v_mfma_f32_16x16x32_f16 v[168:171], v[86:89], v[180:183], v[168:171]
	s_waitcnt lgkmcnt(5)
	v_mfma_f32_16x16x32_f16 v[172:175], v[86:89], v[224:227], v[172:175]
	s_waitcnt lgkmcnt(4)
	v_mfma_f32_16x16x32_f16 v[86:89], v[86:89], v[228:231], v[90:93]
	s_waitcnt vmcnt(14)
	v_mfma_f32_16x16x32_f16 v[232:235], v[140:143], v[94:97], v[232:235]
	v_mfma_f32_16x16x32_f16 v[66:69], v[140:143], v[180:183], v[66:69]
	v_mfma_f32_16x16x32_f16 v[236:239], v[140:143], v[224:227], v[78:81]
	v_mfma_f32_16x16x32_f16 v[70:73], v[140:143], v[228:231], v[70:73]
	s_waitcnt vmcnt(13)
	v_mfma_f32_16x16x32_f16 v[140:143], v[152:155], v[94:97], v[188:191]
	v_mfma_f32_16x16x32_f16 v[74:77], v[152:155], v[180:183], v[74:77]
	v_mfma_f32_16x16x32_f16 v[82:85], v[152:155], v[224:227], v[82:85]
	v_mfma_f32_16x16x32_f16 v[62:65], v[152:155], v[228:231], v[62:65]
	s_waitcnt vmcnt(12)
	v_mfma_f32_16x16x32_f16 v[152:155], v[160:163], v[94:97], v[192:195]
	buffer_load_dwordx4 v[94:97], v147, s[16:19], s8 offen
	buffer_load_dwordx4 v[90:93], v148, s[16:19], s8 offen
	buffer_load_dwordx4 v[78:81], v149, s[16:19], s8 offen
	buffer_load_dwordx4 v[34:37], v150, s[16:19], s8 offen
	v_mfma_f32_16x16x32_f16 v[42:45], v[160:163], v[180:183], v[42:45]
	v_mfma_f32_16x16x32_f16 v[46:49], v[160:163], v[224:227], v[46:49]
	v_mfma_f32_16x16x32_f16 v[160:163], v[160:163], v[228:231], v[196:199]
	v_add_u32_e32 v100, s79, v100
	ds_read_b128 v[180:183], v100
	ds_read_b128 v[188:191], v100 offset:16384
	ds_read_b128 v[192:195], v100 offset:32768
	ds_read_b128 v[196:199], v100 offset:49152
	s_add_i32 s8, s22, s48
	s_waitcnt vmcnt(15) lgkmcnt(7)
	v_mfma_f32_16x16x32_f16 v[164:167], v[126:129], v[204:207], v[164:167]
	s_waitcnt lgkmcnt(6)
	v_mfma_f32_16x16x32_f16 v[168:171], v[126:129], v[208:211], v[168:171]
	s_waitcnt lgkmcnt(5)
	v_mfma_f32_16x16x32_f16 v[172:175], v[126:129], v[212:215], v[172:175]
	s_waitcnt lgkmcnt(4)
	v_mfma_f32_16x16x32_f16 v[86:89], v[126:129], v[216:219], v[86:89]
	s_waitcnt vmcnt(14)
	v_mfma_f32_16x16x32_f16 v[126:129], v[136:139], v[204:207], v[232:235]
	v_mfma_f32_16x16x32_f16 v[66:69], v[136:139], v[208:211], v[66:69]
	v_mfma_f32_16x16x32_f16 v[224:227], v[136:139], v[212:215], v[236:239]
	v_mfma_f32_16x16x32_f16 v[136:139], v[136:139], v[216:219], v[70:73]
	s_waitcnt vmcnt(13)
	v_mfma_f32_16x16x32_f16 v[140:143], v[184:187], v[204:207], v[140:143]
	v_mfma_f32_16x16x32_f16 v[74:77], v[184:187], v[208:211], v[74:77]
	v_mfma_f32_16x16x32_f16 v[228:231], v[184:187], v[212:215], v[82:85]
	v_mfma_f32_16x16x32_f16 v[184:187], v[184:187], v[216:219], v[62:65]
	s_waitcnt vmcnt(12)
	v_mfma_f32_16x16x32_f16 v[152:155], v[200:203], v[204:207], v[152:155]
	v_mfma_f32_16x16x32_f16 v[204:207], v[200:203], v[208:211], v[42:45]
	buffer_load_dwordx4 v[82:85], v147, s[16:19], s8 offen
	buffer_load_dwordx4 v[70:73], v148, s[16:19], s8 offen
	buffer_load_dwordx4 v[62:65], v149, s[16:19], s8 offen
	buffer_load_dwordx4 v[42:45], v150, s[16:19], s8 offen
	v_mfma_f32_16x16x32_f16 v[46:49], v[200:203], v[212:215], v[46:49]
	v_mfma_f32_16x16x32_f16 v[160:163], v[200:203], v[216:219], v[160:163]
	v_add_u32_e32 v0, 0x1ac00, v104
	ds_read_b128 v[240:243], v0
	ds_read_b128 v[244:247], v0 offset:16
	s_waitcnt vmcnt(12) lgkmcnt(5)
	v_mfma_f32_16x16x32_f16 v[164:167], v[122:125], v[180:183], v[164:167]
	v_mfma_f32_16x16x32_f16 v[126:129], v[156:159], v[180:183], v[126:129]
	v_mfma_f32_16x16x32_f16 v[140:143], v[176:179], v[180:183], v[140:143]
	v_mfma_f32_16x16x32_f16 v[152:155], v[220:223], v[180:183], v[152:155]
	s_waitcnt lgkmcnt(4)
	v_mfma_f32_16x16x32_f16 v[168:171], v[122:125], v[188:191], v[168:171]
	v_mfma_f32_16x16x32_f16 v[208:211], v[156:159], v[188:191], v[66:69]
	v_mfma_f32_16x16x32_f16 v[212:215], v[176:179], v[188:191], v[74:77]
	v_mfma_f32_16x16x32_f16 v[204:207], v[220:223], v[188:191], v[204:207]
	s_waitcnt lgkmcnt(3)
	v_mfma_f32_16x16x32_f16 v[172:175], v[122:125], v[192:195], v[172:175]
	v_cvt_pk_f16_f32 v232, v164, v165
	v_cvt_pk_f16_f32 v233, v166, v167
	v_pk_max_f16 v232, v232, 0
	v_pk_max_f16 v233, v233, 0
	v_mfma_f32_16x16x32_f16 v[224:227], v[156:159], v[192:195], v[224:227]
	v_cvt_pk_f16_f32 v234, v126, v127
	v_cvt_pk_f16_f32 v235, v128, v129
	v_pk_max_f16 v234, v234, 0
	v_pk_max_f16 v235, v235, 0
	v_mfma_f32_16x16x32_f16 v[228:231], v[176:179], v[192:195], v[228:231]
	v_cvt_pk_f16_f32 v236, v140, v141
	v_cvt_pk_f16_f32 v237, v142, v143
	v_pk_max_f16 v236, v236, 0
	v_pk_max_f16 v237, v237, 0
	v_mfma_f32_16x16x32_f16 v[216:219], v[220:223], v[192:195], v[46:49]
	v_cvt_pk_f16_f32 v238, v152, v153
	v_cvt_pk_f16_f32 v239, v154, v155
	v_pk_max_f16 v238, v238, 0
	v_pk_max_f16 v239, v239, 0
	s_waitcnt lgkmcnt(2)
	v_mfma_f32_16x16x32_f16 v[200:203], v[122:125], v[196:199], v[86:89]
	v_cvt_pk_f16_f32 v180, v168, v169
	v_cvt_pk_f16_f32 v181, v170, v171
	v_pk_max_f16 v180, v180, 0
	v_pk_max_f16 v181, v181, 0
	s_add_i32 s8, s22, s49
	buffer_load_dwordx4 v[86:89], v147, s[16:19], s8 offen
	buffer_load_dwordx4 v[74:77], v148, s[16:19], s8 offen
	buffer_load_dwordx4 v[66:69], v149, s[16:19], s8 offen
	buffer_load_dwordx4 v[46:49], v150, s[16:19], s8 offen
	v_mfma_f32_16x16x32_f16 v[136:139], v[156:159], v[196:199], v[136:139]
	v_cvt_pk_f16_f32 v182, v208, v209
	v_cvt_pk_f16_f32 v183, v210, v211
	v_pk_max_f16 v182, v182, 0
	v_pk_max_f16 v183, v183, 0
	s_waitcnt lgkmcnt(1)
	v_mfma_f32_16x16x32_f16 v[252:255], v[240:243], v[232:235], 0
	v_cvt_pk_f16_f32 v232, v172, v173
	v_cvt_pk_f16_f32 v233, v174, v175
	v_pk_max_f16 v232, v232, 0
	v_pk_max_f16 v233, v233, 0
	v_mfma_f32_16x16x32_f16 v[184:187], v[176:179], v[196:199], v[184:187]
	v_cvt_pk_f16_f32 v188, v212, v213
	v_cvt_pk_f16_f32 v189, v214, v215
	v_pk_max_f16 v188, v188, 0
	v_pk_max_f16 v189, v189, 0
	s_waitcnt lgkmcnt(0)
	v_mfma_f32_16x16x32_f16 v[252:255], v[244:247], v[236:239], v[252:255]
	ds_read_u16 v102, v114
	ds_read_u16 v103, v114 offset:512
	ds_read_u16 v115, v114 offset:1024
	ds_read_u16 v116, v114 offset:1536
	v_cvt_pk_f16_f32 v234, v224, v225
	v_cvt_pk_f16_f32 v235, v226, v227
	v_pk_max_f16 v234, v234, 0
	v_pk_max_f16 v235, v235, 0
	v_mfma_f32_16x16x32_f16 v[160:163], v[220:223], v[196:199], v[160:163]
	v_cvt_pk_f16_f32 v190, v204, v205
	v_cvt_pk_f16_f32 v191, v206, v207
	v_pk_max_f16 v190, v190, 0
	v_pk_max_f16 v191, v191, 0
	v_mfma_f32_16x16x32_f16 v[192:195], v[240:243], v[180:183], 0
	v_cvt_pk_f16_f32 v236, v228, v229
	v_cvt_pk_f16_f32 v237, v230, v231
	v_pk_max_f16 v236, v236, 0
	v_pk_max_f16 v237, v237, 0
	v_mfma_f32_16x16x32_f16 v[192:195], v[244:247], v[188:191], v[192:195]
	v_cvt_pk_f16_f32 v238, v216, v217
	v_cvt_pk_f16_f32 v239, v218, v219
	v_pk_max_f16 v238, v238, 0
	v_pk_max_f16 v239, v239, 0
	v_cvt_pk_f16_f32 v180, v200, v201
	v_cvt_pk_f16_f32 v181, v202, v203
	v_pk_max_f16 v180, v180, 0
	v_pk_max_f16 v181, v181, 0
	v_mfma_f32_16x16x32_f16 v[196:199], v[240:243], v[232:235], 0
	v_cvt_pk_f16_f32 v182, v136, v137
	v_cvt_pk_f16_f32 v183, v138, v139
	v_pk_max_f16 v182, v182, 0
	v_pk_max_f16 v183, v183, 0
	v_mfma_f32_16x16x32_f16 v[196:199], v[244:247], v[236:239], v[196:199]
	v_cvt_pk_f16_f32 v188, v184, v185
	v_cvt_pk_f16_f32 v189, v186, v187
	v_pk_max_f16 v188, v188, 0
	v_pk_max_f16 v189, v189, 0
	v_cvt_pk_f16_f32 v190, v160, v161
	v_cvt_pk_f16_f32 v191, v162, v163
	v_pk_max_f16 v190, v190, 0
	v_pk_max_f16 v191, v191, 0
	v_mfma_f32_16x16x32_f16 v[122:125], v[240:243], v[180:183], 0
	s_nop 0
	v_mfma_f32_16x16x32_f16 v[122:125], v[244:247], v[188:191], v[122:125]
	v_add_u32_e32 v145, 0x12c00, v105
	ds_read_b128 v[240:243], v145 offset:2048
	ds_read_b128 v[244:247], v145 offset:2064
	ds_read_b128 v[248:251], v145 offset:2080
	s_load_dword s30, s[12:13], 0x0
	v_cndmask_b32_e64 v0, v252, v192, s[2:3]
	ds_read_b128 v[252:255], v145 offset:2096
	v_cndmask_b32_e64 v0, v0, v196, s[0:1]
	v_cndmask_b32_e64 v0, v0, v122, s[26:27]
	ds_write_b32 v112, v0
	s_waitcnt vmcnt(16)
	v_cndmask_b32_e64 v1, v30, v134, s[0:1]
	v_bfi_b32 v30, s10, v1, v30
	v_perm_b32 v1, v22, v134, s24
	v_cndmask_b32_e64 v22, v22, v1, s[0:1]
	v_bfi_b32 v1, s10, v135, v18
	v_perm_b32 v121, v10, v135, s24
	v_cndmask_b32_e64 v18, v18, v1, s[0:1]
	v_cndmask_b32_e64 v10, v10, v121, s[0:1]
	s_add_i32 s22, s22, 0x80000
	s_add_i32 s11, s11, 1
	s_add_u32 s12, s12, 4
	s_addc_u32 s13, s13, 0
	v_add_u32_e32 v104, 0x400, v104
	v_add_u32_e32 v105, 0x800, v105
	v_add_u32_e32 v114, 2, v114
	s_cmp_eq_u32 s22, 0x898000
	s_branch .Lreduce
